# four-waves-per-row version (XCD-grouped rows) with the prep kernel done by 250 working blocks of 5 chunks each, the other 1000 blocks exiting at once
# speedup vs baseline: 1.0452x; 1.0452x over previous
_Z11prep_kernelPKfS0_PfPDv4_DF16_:
	s_cmp_gt_u32 s2, 0xf9
	s_cbranch_scc1 .Lprep_end
	s_load_dwordx4 s[4:7], s[0:1], 0x0
	s_load_dwordx4 s[8:11], s[0:1], 0x10
	s_lshl_b32 s2, s2, 8
	v_add_u32_e32 v2, s2, v0
	v_and_b32_e32 v14, 31, v2
	v_lshlrev_b32_e32 v1, 4, v14
	v_lshlrev_b32_e32 v3, 4, v2
	v_add_u32_e32 v16, 0xfa000, v3
	v_add_u32_e32 v17, 0x1f4000, v3
	v_add_u32_e32 v18, 0x2ee000, v3
	v_add_u32_e32 v19, 0x3e8000, v3
	s_waitcnt lgkmcnt(0)
	global_load_dwordx4 v[4:7], v1, s[6:7]
	global_load_dwordx4 v[8:11], v3, s[4:5]
	global_load_dwordx4 v[20:23], v16, s[4:5]
	global_load_dwordx4 v[24:27], v17, s[4:5]
	global_load_dwordx4 v[28:31], v18, s[4:5]
	global_load_dwordx4 v[32:35], v19, s[4:5]
	v_lshlrev_b32_e32 v13, 3, v2
	v_lshrrev_b32_e32 v12, 5, v2
	v_lshlrev_b32_e32 v15, 2, v12
	s_waitcnt vmcnt(4)
	v_mul_f32_e32 v36, v9, v5
	v_fmac_f32_e32 v36, v8, v4
	v_fmac_f32_e32 v36, v10, v6
	v_fmac_f32_e32 v36, v11, v7
	v_cvt_pk_f16_f32 v8, v8, v9
	v_cvt_pk_f16_f32 v9, v10, v11
	global_store_dwordx2 v13, v[8:9], s[10:11]
	s_waitcnt vmcnt(3)
	v_mul_f32_e32 v37, v21, v5
	v_fmac_f32_e32 v37, v20, v4
	v_fmac_f32_e32 v37, v22, v6
	v_fmac_f32_e32 v37, v23, v7
	v_cvt_pk_f16_f32 v20, v20, v21
	v_cvt_pk_f16_f32 v21, v22, v23
	v_add_u32_e32 v41, 0x7d000, v13
	global_store_dwordx2 v41, v[20:21], s[10:11]
	s_waitcnt vmcnt(2)
	v_mul_f32_e32 v38, v25, v5
	v_fmac_f32_e32 v38, v24, v4
	v_fmac_f32_e32 v38, v26, v6
	v_fmac_f32_e32 v38, v27, v7
	v_cvt_pk_f16_f32 v24, v24, v25
	v_cvt_pk_f16_f32 v25, v26, v27
	v_add_u32_e32 v41, 0xfa000, v13
	global_store_dwordx2 v41, v[24:25], s[10:11]
	s_waitcnt vmcnt(1)
	v_mul_f32_e32 v39, v29, v5
	v_fmac_f32_e32 v39, v28, v4
	v_fmac_f32_e32 v39, v30, v6
	v_fmac_f32_e32 v39, v31, v7
	v_cvt_pk_f16_f32 v28, v28, v29
	v_cvt_pk_f16_f32 v29, v30, v31
	v_add_u32_e32 v41, 0x177000, v13
	global_store_dwordx2 v41, v[28:29], s[10:11]
	s_waitcnt vmcnt(0)
	v_mul_f32_e32 v40, v33, v5
	v_fmac_f32_e32 v40, v32, v4
	v_fmac_f32_e32 v40, v34, v6
	v_fmac_f32_e32 v40, v35, v7
	v_cvt_pk_f16_f32 v32, v32, v33
	v_cvt_pk_f16_f32 v33, v34, v35
	v_add_u32_e32 v41, 0x1f4000, v13
	global_store_dwordx2 v41, v[32:33], s[10:11]
	v_add_f32_dpp v36, v36, v36 quad_perm:[1,0,3,2] row_mask:0xf bank_mask:0xf
	v_add_f32_dpp v37, v37, v37 quad_perm:[1,0,3,2] row_mask:0xf bank_mask:0xf
	v_add_f32_dpp v38, v38, v38 quad_perm:[1,0,3,2] row_mask:0xf bank_mask:0xf
	v_add_f32_dpp v39, v39, v39 quad_perm:[1,0,3,2] row_mask:0xf bank_mask:0xf
	v_add_f32_dpp v40, v40, v40 quad_perm:[1,0,3,2] row_mask:0xf bank_mask:0xf
	v_add_f32_dpp v36, v36, v36 quad_perm:[2,3,0,1] row_mask:0xf bank_mask:0xf
	v_add_f32_dpp v37, v37, v37 quad_perm:[2,3,0,1] row_mask:0xf bank_mask:0xf
	v_add_f32_dpp v38, v38, v38 quad_perm:[2,3,0,1] row_mask:0xf bank_mask:0xf
	v_add_f32_dpp v39, v39, v39 quad_perm:[2,3,0,1] row_mask:0xf bank_mask:0xf
	v_add_f32_dpp v40, v40, v40 quad_perm:[2,3,0,1] row_mask:0xf bank_mask:0xf
	v_add_f32_dpp v36, v36, v36 row_half_mirror row_mask:0xf bank_mask:0xf
	v_add_f32_dpp v37, v37, v37 row_half_mirror row_mask:0xf bank_mask:0xf
	v_add_f32_dpp v38, v38, v38 row_half_mirror row_mask:0xf bank_mask:0xf
	v_add_f32_dpp v39, v39, v39 row_half_mirror row_mask:0xf bank_mask:0xf
	v_add_f32_dpp v40, v40, v40 row_half_mirror row_mask:0xf bank_mask:0xf
	v_add_f32_dpp v36, v36, v36 row_mirror row_mask:0xf bank_mask:0xf
	v_add_f32_dpp v37, v37, v37 row_mirror row_mask:0xf bank_mask:0xf
	v_add_f32_dpp v38, v38, v38 row_mirror row_mask:0xf bank_mask:0xf
	v_add_f32_dpp v39, v39, v39 row_mirror row_mask:0xf bank_mask:0xf
	v_add_f32_dpp v40, v40, v40 row_mirror row_mask:0xf bank_mask:0xf
	v_add_f32_dpp v36, v36, v36 row_bcast:15 row_mask:0xa bank_mask:0xf
	v_add_f32_dpp v37, v37, v37 row_bcast:15 row_mask:0xa bank_mask:0xf
	v_add_f32_dpp v38, v38, v38 row_bcast:15 row_mask:0xa bank_mask:0xf
	v_add_f32_dpp v39, v39, v39 row_bcast:15 row_mask:0xa bank_mask:0xf
	v_add_f32_dpp v40, v40, v40 row_bcast:15 row_mask:0xa bank_mask:0xf
	v_cmp_eq_u32_e32 vcc, 16, v14
	s_and_b64 exec, exec, vcc
	global_store_dword v15, v36, s[8:9]
	v_add_u32_e32 v41, 0x1f40, v15
	global_store_dword v41, v37, s[8:9]
	v_add_u32_e32 v41, 0x3e80, v15
	global_store_dword v41, v38, s[8:9]
	v_add_u32_e32 v41, 0x5dc0, v15
	global_store_dword v41, v39, s[8:9]
	v_add_u32_e32 v41, 0x7d00, v15
	global_store_dword v41, v40, s[8:9]

	.amdhsa_kernel _Z11prep_kernelPKfS0_PfPDv4_DF16_
		.amdhsa_group_segment_fixed_size 0
		.amdhsa_private_segment_fixed_size 0
		.amdhsa_kernarg_size 288
		.amdhsa_user_sgpr_count 2
		.amdhsa_user_sgpr_dispatch_ptr 0
		.amdhsa_user_sgpr_queue_ptr 0
		.amdhsa_user_sgpr_kernarg_segment_ptr 1
		.amdhsa_user_sgpr_dispatch_id 0
		.amdhsa_user_sgpr_kernarg_preload_length 0
		.amdhsa_user_sgpr_kernarg_preload_offset 0
		.amdhsa_user_sgpr_private_segment_size 0
		.amdhsa_uses_dynamic_stack 0
		.amdhsa_enable_private_segment 0
		.amdhsa_system_sgpr_workgroup_id_x 1
		.amdhsa_system_sgpr_workgroup_id_y 0
		.amdhsa_system_sgpr_workgroup_id_z 0
		.amdhsa_system_sgpr_workgroup_info 0
		.amdhsa_system_vgpr_workitem_id 0
		.amdhsa_next_free_vgpr 42
		.amdhsa_next_free_sgpr 14
		.amdhsa_accum_offset 44
		.amdhsa_reserve_vcc 1
		.amdhsa_float_round_mode_32 0
		.amdhsa_float_round_mode_16_64 0
		.amdhsa_float_denorm_mode_32 3
		.amdhsa_float_denorm_mode_16_64 3
		.amdhsa_dx10_clamp 1
		.amdhsa_ieee_mode 1
		.amdhsa_fp16_overflow 0
		.amdhsa_tg_split 0
		.amdhsa_exception_fp_ieee_invalid_op 0
		.amdhsa_exception_fp_denorm_src 0
		.amdhsa_exception_fp_ieee_div_zero 0
		.amdhsa_exception_fp_ieee_overflow 0
		.amdhsa_exception_fp_ieee_underflow 0
		.amdhsa_exception_fp_ieee_inexact 0
		.amdhsa_exception_int_div_zero 0
	.end_amdhsa_kernel

.Lfunc_end0:
	.size	_Z11prep_kernelPKfS0_PfPDv4_DF16_, .Lfunc_end0-_Z11prep_kernelPKfS0_PfPDv4_DF16_
	.set _Z11prep_kernelPKfS0_PfPDv4_DF16_.num_vgpr, 42
	.set _Z11prep_kernelPKfS0_PfPDv4_DF16_.num_agpr, 0
	.set _Z11prep_kernelPKfS0_PfPDv4_DF16_.numbered_sgpr, 14
	.set _Z11prep_kernelPKfS0_PfPDv4_DF16_.num_named_barrier, 0
	.set _Z11prep_kernelPKfS0_PfPDv4_DF16_.private_seg_size, 0
	.set _Z11prep_kernelPKfS0_PfPDv4_DF16_.uses_vcc, 1
	.set _Z11prep_kernelPKfS0_PfPDv4_DF16_.uses_flat_scratch, 0
	.set _Z11prep_kernelPKfS0_PfPDv4_DF16_.has_dyn_sized_stack, 0
	.set _Z11prep_kernelPKfS0_PfPDv4_DF16_.has_recursion, 0
	.set _Z11prep_kernelPKfS0_PfPDv4_DF16_.has_indirect_call, 0

amdhsa.kernels:
  - .agpr_count:     0
    .args:
      - .actual_access:  read_only
        .address_space:  global
        .offset:         0
        .size:           8
        .value_kind:     global_buffer
      - .actual_access:  read_only
        .address_space:  global
        .offset:         8
        .size:           8
        .value_kind:     global_buffer
      - .actual_access:  write_only
        .address_space:  global
        .offset:         16
        .size:           8
        .value_kind:     global_buffer
      - .actual_access:  write_only
        .address_space:  global
        .offset:         24
        .size:           8
        .value_kind:     global_buffer
      - .offset:         32
        .size:           4
        .value_kind:     hidden_block_count_x
      - .offset:         36
        .size:           4
        .value_kind:     hidden_block_count_y
      - .offset:         40
        .size:           4
        .value_kind:     hidden_block_count_z
      - .offset:         44
        .size:           2
        .value_kind:     hidden_group_size_x
      - .offset:         46
        .size:           2
        .value_kind:     hidden_group_size_y
      - .offset:         48
        .size:           2
        .value_kind:     hidden_group_size_z
      - .offset:         50
        .size:           2
        .value_kind:     hidden_remainder_x
      - .offset:         52
        .size:           2
        .value_kind:     hidden_remainder_y
      - .offset:         54
        .size:           2
        .value_kind:     hidden_remainder_z
      - .offset:         72
        .size:           8
        .value_kind:     hidden_global_offset_x
      - .offset:         80
        .size:           8
        .value_kind:     hidden_global_offset_y
      - .offset:         88
        .size:           8
        .value_kind:     hidden_global_offset_z
      - .offset:         96
        .size:           2
        .value_kind:     hidden_grid_dims
    .group_segment_fixed_size: 0
    .kernarg_segment_align: 8
    .kernarg_segment_size: 288
    .language:       OpenCL C
    .language_version:
      - 2
      - 0
    .max_flat_workgroup_size: 256
    .name:           _Z11prep_kernelPKfS0_PfPDv4_DF16_
    .private_segment_fixed_size: 0
    .sgpr_count:     20
    .sgpr_spill_count: 0
    .symbol:         _Z11prep_kernelPKfS0_PfPDv4_DF16_.kd
    .uniform_work_group_size: 1
    .uses_dynamic_stack: false
    .vgpr_count:     42
    .vgpr_spill_count: 0
    .wavefront_size: 64
  - .agpr_count:     0
    .args:
      - .actual_access:  read_only
        .address_space:  global
        .offset:         0
        .size:           8
        .value_kind:     global_buffer
      - .actual_access:  read_only
        .address_space:  global
        .offset:         8
        .size:           8
        .value_kind:     global_buffer
      - .actual_access:  read_only
        .address_space:  global
        .offset:         16
        .size:           8
        .value_kind:     global_buffer
      - .actual_access:  read_only
        .address_space:  global
        .offset:         24
        .size:           8
        .value_kind:     global_buffer
      - .actual_access:  write_only
        .address_space:  global
        .offset:         32
        .size:           8
        .value_kind:     global_buffer
      - .offset:         40
        .size:           4
        .value_kind:     by_value
    .group_segment_fixed_size: 36928
    .kernarg_segment_align: 8
    .kernarg_segment_size: 44
    .language:       OpenCL C
    .language_version:
      - 2
      - 0
    .max_flat_workgroup_size: 512
    .name:           _Z11attn_kernelPKfS0_PKDv8_DF16_S0_Pfi
    .private_segment_fixed_size: 0
    .sgpr_count:     64
    .sgpr_spill_count: 0
    .symbol:         _Z11attn_kernelPKfS0_PKDv8_DF16_S0_Pfi.kd
    .uniform_work_group_size: 1
    .uses_dynamic_stack: false
    .vgpr_count:     248
    .vgpr_spill_count: 0
    .wavefront_size: 64
